# out-projection GEMM (phase E) epilogue: serialized 32x(2 loads, vmcnt(0), fma, store) chain replaced by 4 batches of 8 xin loads + gate loaded once per unit
# speedup vs baseline: 1.0118x; 1.0118x over previous
.LBB0_1287:
	ds_read_b128 v[144:147], v150
	ds_read_b128 v[154:157], v150 offset:1024
	ds_read_b128 v[158:161], v150 offset:2048
	ds_read_b128 v[162:165], v150 offset:3072
	s_add_u32 s24, s22, 0xfff80080
	s_addc_u32 s25, s23, -1
	s_cmp_eq_u32 s53, 28
	s_cselect_b32 s27, s15, s25
	s_cselect_b32 s26, s49, s24
	s_cselect_b32 s25, s13, s52
	s_cselect_b32 s24, s50, s51
	v_lshl_add_u64 v[190:191], s[22:23], 0, v[136:137]
	s_add_i32 m0, s21, 0xc000
	ds_read_b128 v[166:169], v151
	ds_read_b128 v[170:173], v151 offset:1024
	ds_read_b128 v[174:177], v151 offset:2048
	ds_read_b128 v[178:181], v151 offset:3072
	ds_read_b128 v[182:185], v151 offset:4096
	ds_read_b128 v[186:189], v151 offset:5120
	ds_read_b128 v[192:195], v151 offset:6144
	ds_read_b128 v[196:199], v151 offset:7168
	global_load_lds_dwordx4 v[190:191], off
	v_lshl_add_u64 v[190:191], s[22:23], 0, v[138:139]
	s_add_i32 m0, s21, 0xe000
	s_nop 0
	global_load_lds_dwordx4 v[190:191], off
	s_waitcnt lgkmcnt(8)
	s_barrier
	s_waitcnt lgkmcnt(0)
	s_setprio 1
	s_waitcnt lgkmcnt(0)
	v_mfma_f32_16x16x32_bf16 v[126:129], v[144:147], v[166:169], v[126:129]
	v_mfma_f32_16x16x32_bf16 v[122:125], v[158:161], v[166:169], v[122:125]
	v_mfma_f32_16x16x32_bf16 v[114:117], v[144:147], v[174:177], v[114:117]
	v_mfma_f32_16x16x32_bf16 v[106:109], v[158:161], v[174:177], v[106:109]
	v_mfma_f32_16x16x32_bf16 v[98:101], v[144:147], v[182:185], v[98:101]
	v_mfma_f32_16x16x32_bf16 v[90:93], v[158:161], v[182:185], v[90:93]
	v_mfma_f32_16x16x32_bf16 v[82:85], v[144:147], v[192:195], v[82:85]
	v_mfma_f32_16x16x32_bf16 v[74:77], v[158:161], v[192:195], v[74:77]
	v_mfma_f32_16x16x32_bf16 v[126:129], v[154:157], v[170:173], v[126:129]
	v_mfma_f32_16x16x32_bf16 v[122:125], v[162:165], v[170:173], v[122:125]
	v_mfma_f32_16x16x32_bf16 v[114:117], v[154:157], v[178:181], v[114:117]
	v_mfma_f32_16x16x32_bf16 v[106:109], v[162:165], v[178:181], v[106:109]
	v_mfma_f32_16x16x32_bf16 v[98:101], v[154:157], v[186:189], v[98:101]
	v_mfma_f32_16x16x32_bf16 v[90:93], v[162:165], v[186:189], v[90:93]
	v_mfma_f32_16x16x32_bf16 v[82:85], v[154:157], v[196:199], v[82:85]
	v_mfma_f32_16x16x32_bf16 v[74:77], v[162:165], v[196:199], v[74:77]
	s_setprio 0
	s_barrier
	s_add_i32 s54, s45, s36
	v_lshl_add_u64 v[190:191], s[24:25], 0, v[132:133]
	s_mov_b32 m0, s54
	ds_read_b128 v[200:203], v152
	ds_read_b128 v[204:207], v152 offset:1024
	ds_read_b128 v[208:211], v152 offset:2048
	ds_read_b128 v[212:215], v152 offset:3072
	global_load_lds_dwordx4 v[190:191], off
	v_lshl_add_u64 v[216:217], s[24:25], 0, v[130:131]
	s_add_i32 m0, s54, 0x2000
	s_nop 0
	global_load_lds_dwordx4 v[216:217], off
	s_barrier
	s_waitcnt lgkmcnt(0)
	s_setprio 1
	s_waitcnt lgkmcnt(0)
	v_mfma_f32_16x16x32_bf16 v[118:121], v[200:203], v[166:169], v[118:121]
	v_mfma_f32_16x16x32_bf16 v[110:113], v[208:211], v[166:169], v[110:113]
	v_mfma_f32_16x16x32_bf16 v[102:105], v[200:203], v[174:177], v[102:105]
	v_mfma_f32_16x16x32_bf16 v[94:97], v[208:211], v[174:177], v[94:97]
	v_mfma_f32_16x16x32_bf16 v[86:89], v[200:203], v[182:185], v[86:89]
	v_mfma_f32_16x16x32_bf16 v[78:81], v[208:211], v[182:185], v[78:81]
	v_mfma_f32_16x16x32_bf16 v[70:73], v[200:203], v[192:195], v[70:73]
	v_mfma_f32_16x16x32_bf16 v[66:69], v[208:211], v[192:195], v[66:69]
	v_mfma_f32_16x16x32_bf16 v[118:121], v[204:207], v[170:173], v[118:121]
	v_mfma_f32_16x16x32_bf16 v[110:113], v[212:215], v[170:173], v[110:113]
	v_mfma_f32_16x16x32_bf16 v[102:105], v[204:207], v[178:181], v[102:105]
	v_mfma_f32_16x16x32_bf16 v[94:97], v[212:215], v[178:181], v[94:97]
	v_mfma_f32_16x16x32_bf16 v[86:89], v[204:207], v[186:189], v[86:89]
	v_mfma_f32_16x16x32_bf16 v[78:81], v[212:215], v[186:189], v[78:81]
	v_mfma_f32_16x16x32_bf16 v[70:73], v[204:207], v[196:199], v[70:73]
	v_mfma_f32_16x16x32_bf16 v[66:69], v[212:215], v[196:199], v[66:69]
	s_setprio 0
	s_mov_b32 m0, s21
	v_lshl_add_u64 v[218:219], s[26:27], 0, v[132:133]
	s_barrier
	ds_read_b128 v[166:169], v151 offset:16384
	ds_read_b128 v[170:173], v151 offset:17408
	ds_read_b128 v[174:177], v151 offset:18432
	ds_read_b128 v[178:181], v151 offset:19456
	ds_read_b128 v[182:185], v151 offset:20480
	ds_read_b128 v[186:189], v151 offset:21504
	ds_read_b128 v[192:195], v151 offset:22528
	ds_read_b128 v[196:199], v151 offset:23552
	global_load_lds_dwordx4 v[218:219], off
	v_lshl_add_u64 v[220:221], s[26:27], 0, v[130:131]
	s_mov_b32 m0, s38
	s_nop 0
	global_load_lds_dwordx4 v[220:221], off
	s_barrier
	s_waitcnt lgkmcnt(0)
	s_setprio 1
	s_waitcnt lgkmcnt(0)
	v_mfma_f32_16x16x32_bf16 v[62:65], v[144:147], v[166:169], v[62:65]
	v_mfma_f32_16x16x32_bf16 v[58:61], v[158:161], v[166:169], v[58:61]
	v_mfma_f32_16x16x32_bf16 v[50:53], v[144:147], v[174:177], v[50:53]
	v_mfma_f32_16x16x32_bf16 v[42:45], v[158:161], v[174:177], v[42:45]
	v_mfma_f32_16x16x32_bf16 v[34:37], v[144:147], v[182:185], v[34:37]
	v_mfma_f32_16x16x32_bf16 v[26:29], v[158:161], v[182:185], v[26:29]
	v_mfma_f32_16x16x32_bf16 v[18:21], v[144:147], v[192:195], v[18:21]
	v_mfma_f32_16x16x32_bf16 v[10:13], v[158:161], v[192:195], v[10:13]
	v_mfma_f32_16x16x32_bf16 v[62:65], v[154:157], v[170:173], v[62:65]
	v_mfma_f32_16x16x32_bf16 v[58:61], v[162:165], v[170:173], v[58:61]
	v_mfma_f32_16x16x32_bf16 v[50:53], v[154:157], v[178:181], v[50:53]
	v_mfma_f32_16x16x32_bf16 v[42:45], v[162:165], v[178:181], v[42:45]
	v_mfma_f32_16x16x32_bf16 v[34:37], v[154:157], v[186:189], v[34:37]
	v_mfma_f32_16x16x32_bf16 v[26:29], v[162:165], v[186:189], v[26:29]
	v_mfma_f32_16x16x32_bf16 v[18:21], v[154:157], v[196:199], v[18:21]
	v_mfma_f32_16x16x32_bf16 v[10:13], v[162:165], v[196:199], v[10:13]
	s_setprio 0
	s_barrier
	s_add_u32 s54, s24, 0x80000
	s_addc_u32 s55, s25, 0
	s_add_i32 s56, s46, s36
	v_lshl_add_u64 v[144:145], s[54:55], 0, v[132:133]
	s_mov_b32 m0, s56
	s_nop 0
	global_load_lds_dwordx4 v[144:145], off
	v_lshl_add_u64 v[144:145], s[54:55], 0, v[130:131]
	s_add_i32 m0, s56, 0x2000
	s_nop 0
	global_load_lds_dwordx4 v[144:145], off
	s_waitcnt vmcnt(6)
	s_barrier
	s_setprio 1
	v_mfma_f32_16x16x32_bf16 v[54:57], v[200:203], v[166:169], v[54:57]
	v_mfma_f32_16x16x32_bf16 v[46:49], v[208:211], v[166:169], v[46:49]
	v_mfma_f32_16x16x32_bf16 v[38:41], v[200:203], v[174:177], v[38:41]
	v_mfma_f32_16x16x32_bf16 v[30:33], v[208:211], v[174:177], v[30:33]
	v_mfma_f32_16x16x32_bf16 v[22:25], v[200:203], v[182:185], v[22:25]
	v_mfma_f32_16x16x32_bf16 v[14:17], v[208:211], v[182:185], v[14:17]
	v_mfma_f32_16x16x32_bf16 v[6:9], v[200:203], v[192:195], v[6:9]
	v_mfma_f32_16x16x32_bf16 v[2:5], v[208:211], v[192:195], v[2:5]
	v_mfma_f32_16x16x32_bf16 v[54:57], v[204:207], v[170:173], v[54:57]
	v_mfma_f32_16x16x32_bf16 v[46:49], v[212:215], v[170:173], v[46:49]
	v_mfma_f32_16x16x32_bf16 v[38:41], v[204:207], v[178:181], v[38:41]
	v_mfma_f32_16x16x32_bf16 v[30:33], v[212:215], v[178:181], v[30:33]
	v_mfma_f32_16x16x32_bf16 v[22:25], v[204:207], v[186:189], v[22:25]
	v_mfma_f32_16x16x32_bf16 v[14:17], v[212:215], v[186:189], v[14:17]
	v_mfma_f32_16x16x32_bf16 v[6:9], v[204:207], v[196:199], v[6:9]
	v_mfma_f32_16x16x32_bf16 v[2:5], v[212:215], v[196:199], v[2:5]
	s_setprio 0
	s_add_i32 s54, 0, 0x18000
	v_add_u32_e32 v134, s54, v148
	s_barrier
	ds_read_b128 v[144:147], v134
	ds_read_b128 v[154:157], v134 offset:1024
	ds_read_b128 v[158:161], v134 offset:2048
	ds_read_b128 v[162:165], v134 offset:3072
	s_add_u32 s26, s26, 0x80000
	s_addc_u32 s27, s27, 0
	s_mov_b32 m0, s39
	v_lshl_add_u64 v[200:201], s[26:27], 0, v[132:133]
	ds_read_b128 v[166:169], v151 offset:32768
	ds_read_b128 v[170:173], v151 offset:33792
	ds_read_b128 v[174:177], v151 offset:34816
	ds_read_b128 v[178:181], v151 offset:35840
	ds_read_b128 v[182:185], v151 offset:36864
	ds_read_b128 v[186:189], v151 offset:37888
	ds_read_b128 v[192:195], v151 offset:38912
	ds_read_b128 v[196:199], v151 offset:39936
	global_load_lds_dwordx4 v[200:201], off
	v_lshl_add_u64 v[200:201], s[26:27], 0, v[130:131]
	s_mov_b32 m0, s40
	s_nop 0
	global_load_lds_dwordx4 v[200:201], off
	s_waitcnt lgkmcnt(8)
	s_barrier
	s_waitcnt lgkmcnt(0)
	s_setprio 1
	s_waitcnt lgkmcnt(0)
	v_mfma_f32_16x16x32_bf16 v[126:129], v[144:147], v[166:169], v[126:129]
	v_mfma_f32_16x16x32_bf16 v[122:125], v[158:161], v[166:169], v[122:125]
	v_mfma_f32_16x16x32_bf16 v[114:117], v[144:147], v[174:177], v[114:117]
	v_mfma_f32_16x16x32_bf16 v[106:109], v[158:161], v[174:177], v[106:109]
	v_mfma_f32_16x16x32_bf16 v[98:101], v[144:147], v[182:185], v[98:101]
	v_mfma_f32_16x16x32_bf16 v[90:93], v[158:161], v[182:185], v[90:93]
	v_mfma_f32_16x16x32_bf16 v[82:85], v[144:147], v[192:195], v[82:85]
	v_mfma_f32_16x16x32_bf16 v[74:77], v[158:161], v[192:195], v[74:77]
	v_mfma_f32_16x16x32_bf16 v[126:129], v[154:157], v[170:173], v[126:129]
	v_mfma_f32_16x16x32_bf16 v[122:125], v[162:165], v[170:173], v[122:125]
	v_mfma_f32_16x16x32_bf16 v[114:117], v[154:157], v[178:181], v[114:117]
	v_mfma_f32_16x16x32_bf16 v[106:109], v[162:165], v[178:181], v[106:109]
	v_mfma_f32_16x16x32_bf16 v[98:101], v[154:157], v[186:189], v[98:101]
	v_mfma_f32_16x16x32_bf16 v[90:93], v[162:165], v[186:189], v[90:93]
	v_mfma_f32_16x16x32_bf16 v[82:85], v[154:157], v[196:199], v[82:85]
	v_mfma_f32_16x16x32_bf16 v[74:77], v[162:165], v[196:199], v[74:77]
	s_setprio 0
	s_barrier
	s_add_i32 s26, 0, 0x1c000
	s_add_i32 s27, s54, s36
	v_add_u32_e32 v134, s26, v148
	v_lshl_add_u64 v[190:191], v[190:191], 0, s[6:7]
	s_mov_b32 m0, s27
	ds_read_b128 v[200:203], v134
	ds_read_b128 v[204:207], v134 offset:1024
	ds_read_b128 v[208:211], v134 offset:2048
	ds_read_b128 v[212:215], v134 offset:3072
	global_load_lds_dwordx4 v[190:191], off
	v_lshl_add_u64 v[190:191], v[216:217], 0, s[6:7]
	s_add_i32 m0, s27, 0x2000
	s_nop 0
	global_load_lds_dwordx4 v[190:191], off
	s_barrier
	s_waitcnt lgkmcnt(0)
	s_setprio 1
	s_waitcnt lgkmcnt(0)
	v_mfma_f32_16x16x32_bf16 v[118:121], v[200:203], v[166:169], v[118:121]
	v_mfma_f32_16x16x32_bf16 v[110:113], v[208:211], v[166:169], v[110:113]
	v_mfma_f32_16x16x32_bf16 v[102:105], v[200:203], v[174:177], v[102:105]
	v_mfma_f32_16x16x32_bf16 v[94:97], v[208:211], v[174:177], v[94:97]
	v_mfma_f32_16x16x32_bf16 v[86:89], v[200:203], v[182:185], v[86:89]
	v_mfma_f32_16x16x32_bf16 v[78:81], v[208:211], v[182:185], v[78:81]
	v_mfma_f32_16x16x32_bf16 v[70:73], v[200:203], v[192:195], v[70:73]
	v_mfma_f32_16x16x32_bf16 v[66:69], v[208:211], v[192:195], v[66:69]
	v_mfma_f32_16x16x32_bf16 v[118:121], v[204:207], v[170:173], v[118:121]
	v_mfma_f32_16x16x32_bf16 v[110:113], v[212:215], v[170:173], v[110:113]
	v_mfma_f32_16x16x32_bf16 v[102:105], v[204:207], v[178:181], v[102:105]
	v_mfma_f32_16x16x32_bf16 v[94:97], v[212:215], v[178:181], v[94:97]
	v_mfma_f32_16x16x32_bf16 v[86:89], v[204:207], v[186:189], v[86:89]
	v_mfma_f32_16x16x32_bf16 v[78:81], v[212:215], v[186:189], v[78:81]
	v_mfma_f32_16x16x32_bf16 v[70:73], v[204:207], v[196:199], v[70:73]
	v_mfma_f32_16x16x32_bf16 v[66:69], v[212:215], v[196:199], v[66:69]
	s_setprio 0
	s_mov_b32 m0, s42
	v_lshl_add_u64 v[190:191], v[218:219], 0, s[6:7]
	s_barrier
	ds_read_b128 v[166:169], v151 offset:49152
	ds_read_b128 v[170:173], v151 offset:50176
	ds_read_b128 v[174:177], v151 offset:51200
	ds_read_b128 v[178:181], v151 offset:52224
	ds_read_b128 v[182:185], v151 offset:53248
	ds_read_b128 v[186:189], v151 offset:54272
	ds_read_b128 v[192:195], v151 offset:55296
	ds_read_b128 v[196:199], v151 offset:56320
	global_load_lds_dwordx4 v[190:191], off
	v_lshl_add_u64 v[190:191], v[220:221], 0, s[6:7]
	s_mov_b32 m0, s43
	s_nop 0
	global_load_lds_dwordx4 v[190:191], off
	s_barrier
	s_waitcnt lgkmcnt(0)
	s_setprio 1
	s_waitcnt lgkmcnt(0)
	v_mfma_f32_16x16x32_bf16 v[62:65], v[144:147], v[166:169], v[62:65]
	v_mfma_f32_16x16x32_bf16 v[58:61], v[158:161], v[166:169], v[58:61]
	v_mfma_f32_16x16x32_bf16 v[50:53], v[144:147], v[174:177], v[50:53]
	v_mfma_f32_16x16x32_bf16 v[42:45], v[158:161], v[174:177], v[42:45]
	v_mfma_f32_16x16x32_bf16 v[34:37], v[144:147], v[182:185], v[34:37]
	v_mfma_f32_16x16x32_bf16 v[26:29], v[158:161], v[182:185], v[26:29]
	v_mfma_f32_16x16x32_bf16 v[18:21], v[144:147], v[192:195], v[18:21]
	v_mfma_f32_16x16x32_bf16 v[10:13], v[158:161], v[192:195], v[10:13]
	v_mfma_f32_16x16x32_bf16 v[62:65], v[154:157], v[170:173], v[62:65]
	v_mfma_f32_16x16x32_bf16 v[58:61], v[162:165], v[170:173], v[58:61]
	v_mfma_f32_16x16x32_bf16 v[50:53], v[154:157], v[178:181], v[50:53]
	v_mfma_f32_16x16x32_bf16 v[42:45], v[162:165], v[178:181], v[42:45]
	v_mfma_f32_16x16x32_bf16 v[34:37], v[154:157], v[186:189], v[34:37]
	v_mfma_f32_16x16x32_bf16 v[26:29], v[162:165], v[186:189], v[26:29]
	v_mfma_f32_16x16x32_bf16 v[18:21], v[154:157], v[196:199], v[18:21]
	v_mfma_f32_16x16x32_bf16 v[10:13], v[162:165], v[196:199], v[10:13]
	s_setprio 0
	s_barrier
	s_add_u32 s24, s24, 0x80080
	s_addc_u32 s25, s25, 0
	s_add_i32 s26, s26, s36
	v_lshl_add_u64 v[144:145], s[24:25], 0, v[132:133]
	s_mov_b32 m0, s26
	s_nop 0
	global_load_lds_dwordx4 v[144:145], off
	v_lshl_add_u64 v[144:145], s[24:25], 0, v[130:131]
	s_add_i32 m0, s26, 0x2000
	s_nop 0
	global_load_lds_dwordx4 v[144:145], off
	s_waitcnt vmcnt(6)
	s_barrier
	s_setprio 1
	v_mfma_f32_16x16x32_bf16 v[54:57], v[200:203], v[166:169], v[54:57]
	v_mfma_f32_16x16x32_bf16 v[46:49], v[208:211], v[166:169], v[46:49]
	v_mfma_f32_16x16x32_bf16 v[38:41], v[200:203], v[174:177], v[38:41]
	v_mfma_f32_16x16x32_bf16 v[30:33], v[208:211], v[174:177], v[30:33]
	v_mfma_f32_16x16x32_bf16 v[22:25], v[200:203], v[182:185], v[22:25]
	v_mfma_f32_16x16x32_bf16 v[14:17], v[208:211], v[182:185], v[14:17]
	v_mfma_f32_16x16x32_bf16 v[6:9], v[200:203], v[192:195], v[6:9]
	v_mfma_f32_16x16x32_bf16 v[2:5], v[208:211], v[192:195], v[2:5]
	v_mfma_f32_16x16x32_bf16 v[54:57], v[204:207], v[170:173], v[54:57]
	v_mfma_f32_16x16x32_bf16 v[46:49], v[212:215], v[170:173], v[46:49]
	v_mfma_f32_16x16x32_bf16 v[38:41], v[204:207], v[178:181], v[38:41]
	v_mfma_f32_16x16x32_bf16 v[30:33], v[212:215], v[178:181], v[30:33]
	v_mfma_f32_16x16x32_bf16 v[22:25], v[204:207], v[186:189], v[22:25]
	v_mfma_f32_16x16x32_bf16 v[14:17], v[212:215], v[186:189], v[14:17]
	v_mfma_f32_16x16x32_bf16 v[6:9], v[204:207], v[196:199], v[6:9]
	v_mfma_f32_16x16x32_bf16 v[2:5], v[212:215], v[196:199], v[2:5]
	s_setprio 0
	s_add_i32 s53, s53, 2
	s_add_u32 s22, s22, 0x100
	s_addc_u32 s23, s23, 0
	s_add_u32 s51, s51, 0x100
	s_addc_u32 s52, s52, 0
	s_cmp_gt_u32 s53, 29
	s_barrier
	s_cbranch_scc0 .LBB0_1287
	v_lshl_add_u32 v144, s20, 8, v1
	s_movk_i32 s13, 0x4000
	v_lshl_or_b32 v146, s48, 8, v149
	v_ashrrev_i32_e32 v134, 31, v144
	v_cmp_gt_i32_e32 vcc, s13, v144
	v_readlane_b32 s48, v250, 7
	v_add_u32_e32 v154, 0xffffc000, v144
	v_cndmask_b32_e32 v145, 0, v134, vcc
	v_readlane_b32 s49, v250, 8
	v_readlane_b32 s52, v250, 11
	v_readlane_b32 s53, v250, 12
	v_cndmask_b32_e32 v158, v154, v144, vcc
	v_mov_b32_e32 v159, v145
	v_mov_b32_e32 v154, s53
	v_mov_b32_e32 v155, s49
	v_mov_b32_e32 v156, s52
	v_mov_b32_e32 v157, s48
	s_movk_i32 s13, 0x3fff
	v_ashrrev_i32_e32 v147, 31, v146
	v_cndmask_b32_e32 v161, v154, v155, vcc
	v_cndmask_b32_e32 v160, v156, v157, vcc
	v_lshlrev_b64 v[158:159], 13, v[158:159]
	v_cmp_lt_i32_e32 vcc, s13, v144
	v_lshl_add_u64 v[158:159], v[160:161], 0, v[158:159]
	v_lshlrev_b64 v[146:147], 2, v[146:147]
	v_cndmask_b32_e32 v134, 0, v153, vcc
	v_lshl_add_u64 v[166:167], v[158:159], 0, v[146:147]
	v_lshl_add_u64 v[158:159], s[4:5], 0, v[134:135]
	v_lshl_add_u64 v[168:169], v[158:159], 0, v[146:147]
	v_add_co_u32_e32 v158, vcc, s47, v168
	v_lshlrev_b64 v[170:171], 13, v[144:145]
	s_nop 0
	v_addc_co_u32_e32 v159, vcc, 0, v169, vcc
	v_lshl_add_u64 v[170:171], s[8:9], 0, v[170:171]
	v_lshl_add_u64 v[170:171], v[170:171], 0, v[146:147]
	v_lshl_add_u64 v[168:169], v[168:169], 0, s[10:11]
	global_load_dwordx4 v[144:147], v[158:159], off
	global_load_dwordx4 v[154:157], v[168:169], off offset:64
	global_load_dwordx4 v[160:163], v[168:169], off offset:512
	global_load_dwordx4 v[172:175], v[168:169], off offset:576
	global_load_dwordx4 v[176:179], v[166:167], off
	global_load_dwordx4 v[180:183], v[166:167], off offset:64
	global_load_dwordx4 v[184:187], v[166:167], off offset:512
	global_load_dwordx4 v[192:195], v[166:167], off offset:576
	v_add_co_u32_e32 v188, vcc, 0x20000, v166
	s_nop 1
	v_addc_co_u32_e32 v189, vcc, 0, v167, vcc
	global_load_dwordx4 v[196:199], v[188:189], off
	global_load_dwordx4 v[200:203], v[188:189], off offset:64
	global_load_dwordx4 v[204:207], v[188:189], off offset:512
	global_load_dwordx4 v[208:211], v[188:189], off offset:576
	v_add_co_u32_e32 v214, vcc, 0x20000, v170
	s_nop 1
	v_addc_co_u32_e32 v215, vcc, 0, v171, vcc
	s_waitcnt vmcnt(0)
	v_pk_fma_f32 v[128:129], v[128:129], v[146:147], v[178:179]
	v_pk_fma_f32 v[126:127], v[126:127], v[144:145], v[176:177]
	global_store_dwordx4 v[170:171], v[126:129], off
	v_pk_fma_f32 v[124:125], v[124:125], v[156:157], v[182:183]
	v_pk_fma_f32 v[122:123], v[122:123], v[154:155], v[180:181]
	global_store_dwordx4 v[170:171], v[122:125], off offset:64
	v_pk_fma_f32 v[120:121], v[120:121], v[162:163], v[186:187]
	v_pk_fma_f32 v[118:119], v[118:119], v[160:161], v[184:185]
	global_store_dwordx4 v[170:171], v[118:121], off offset:512
	v_pk_fma_f32 v[112:113], v[112:113], v[174:175], v[194:195]
	v_pk_fma_f32 v[110:111], v[110:111], v[172:173], v[192:193]
	global_store_dwordx4 v[170:171], v[110:113], off offset:576
	v_pk_fma_f32 v[116:117], v[116:117], v[146:147], v[198:199]
	v_pk_fma_f32 v[114:115], v[114:115], v[144:145], v[196:197]
	global_store_dwordx4 v[214:215], v[114:117], off
	v_pk_fma_f32 v[108:109], v[108:109], v[156:157], v[202:203]
	v_pk_fma_f32 v[106:107], v[106:107], v[154:155], v[200:201]
	global_store_dwordx4 v[214:215], v[106:109], off offset:64
	v_pk_fma_f32 v[104:105], v[104:105], v[162:163], v[206:207]
	v_pk_fma_f32 v[102:103], v[102:103], v[160:161], v[204:205]
	global_store_dwordx4 v[214:215], v[102:105], off offset:512
	v_pk_fma_f32 v[96:97], v[96:97], v[174:175], v[210:211]
	v_pk_fma_f32 v[94:95], v[94:95], v[172:173], v[208:209]
	global_store_dwordx4 v[214:215], v[94:97], off offset:576
	v_add_co_u32_e32 v164, vcc, 0x40000, v166
	s_nop 1
	v_addc_co_u32_e32 v165, vcc, 0, v167, vcc
	global_load_dwordx4 v[176:179], v[164:165], off
	global_load_dwordx4 v[180:183], v[164:165], off offset:64
	global_load_dwordx4 v[184:187], v[164:165], off offset:512
	global_load_dwordx4 v[192:195], v[164:165], off offset:576
	v_add_co_u32_e32 v188, vcc, 0x60000, v166
	s_nop 1
	v_addc_co_u32_e32 v189, vcc, 0, v167, vcc
	global_load_dwordx4 v[196:199], v[188:189], off
	global_load_dwordx4 v[200:203], v[188:189], off offset:64
	global_load_dwordx4 v[204:207], v[188:189], off offset:512
	global_load_dwordx4 v[208:211], v[188:189], off offset:576
	v_add_co_u32_e32 v212, vcc, 0x40000, v170
	s_nop 1
	v_addc_co_u32_e32 v213, vcc, 0, v171, vcc
	v_add_co_u32_e32 v214, vcc, 0x60000, v170
	s_nop 1
	v_addc_co_u32_e32 v215, vcc, 0, v171, vcc
	s_waitcnt vmcnt(0)
	v_pk_fma_f32 v[100:101], v[100:101], v[146:147], v[178:179]
	v_pk_fma_f32 v[98:99], v[98:99], v[144:145], v[176:177]
	global_store_dwordx4 v[212:213], v[98:101], off
	v_pk_fma_f32 v[92:93], v[92:93], v[156:157], v[182:183]
	v_pk_fma_f32 v[90:91], v[90:91], v[154:155], v[180:181]
	global_store_dwordx4 v[212:213], v[90:93], off offset:64
	v_pk_fma_f32 v[88:89], v[88:89], v[162:163], v[186:187]
	v_pk_fma_f32 v[86:87], v[86:87], v[160:161], v[184:185]
	global_store_dwordx4 v[212:213], v[86:89], off offset:512
	v_pk_fma_f32 v[80:81], v[80:81], v[174:175], v[194:195]
	v_pk_fma_f32 v[78:79], v[78:79], v[172:173], v[192:193]
	global_store_dwordx4 v[212:213], v[78:81], off offset:576
	v_pk_fma_f32 v[84:85], v[84:85], v[146:147], v[198:199]
	v_pk_fma_f32 v[82:83], v[82:83], v[144:145], v[196:197]
	global_store_dwordx4 v[214:215], v[82:85], off
	v_pk_fma_f32 v[76:77], v[76:77], v[156:157], v[202:203]
	v_pk_fma_f32 v[74:75], v[74:75], v[154:155], v[200:201]
	global_store_dwordx4 v[214:215], v[74:77], off offset:64
	v_pk_fma_f32 v[72:73], v[72:73], v[162:163], v[206:207]
	v_pk_fma_f32 v[70:71], v[70:71], v[160:161], v[204:205]
	global_store_dwordx4 v[214:215], v[70:73], off offset:512
	v_pk_fma_f32 v[68:69], v[68:69], v[174:175], v[210:211]
	v_pk_fma_f32 v[66:67], v[66:67], v[172:173], v[208:209]
	global_store_dwordx4 v[214:215], v[66:69], off offset:576
	v_add_co_u32_e32 v164, vcc, 0x100000, v166
	s_nop 1
	v_addc_co_u32_e32 v165, vcc, 0, v167, vcc
	global_load_dwordx4 v[176:179], v[164:165], off
	global_load_dwordx4 v[180:183], v[164:165], off offset:64
	global_load_dwordx4 v[184:187], v[164:165], off offset:512
	global_load_dwordx4 v[192:195], v[164:165], off offset:576
	v_add_co_u32_e32 v188, vcc, 0x120000, v166
	s_nop 1
	v_addc_co_u32_e32 v189, vcc, 0, v167, vcc
	global_load_dwordx4 v[196:199], v[188:189], off
	global_load_dwordx4 v[200:203], v[188:189], off offset:64
	global_load_dwordx4 v[204:207], v[188:189], off offset:512
	global_load_dwordx4 v[208:211], v[188:189], off offset:576
	v_add_co_u32_e32 v212, vcc, 0x100000, v170
	s_nop 1
	v_addc_co_u32_e32 v213, vcc, 0, v171, vcc
	v_add_co_u32_e32 v214, vcc, 0x120000, v170
	s_nop 1
	v_addc_co_u32_e32 v215, vcc, 0, v171, vcc
	s_waitcnt vmcnt(0)
	v_pk_fma_f32 v[64:65], v[64:65], v[146:147], v[178:179]
	v_pk_fma_f32 v[62:63], v[62:63], v[144:145], v[176:177]
	global_store_dwordx4 v[212:213], v[62:65], off
	v_pk_fma_f32 v[60:61], v[60:61], v[156:157], v[182:183]
	v_pk_fma_f32 v[58:59], v[58:59], v[154:155], v[180:181]
	global_store_dwordx4 v[212:213], v[58:61], off offset:64
	v_pk_fma_f32 v[56:57], v[56:57], v[162:163], v[186:187]
	v_pk_fma_f32 v[54:55], v[54:55], v[160:161], v[184:185]
	global_store_dwordx4 v[212:213], v[54:57], off offset:512
	v_pk_fma_f32 v[48:49], v[48:49], v[174:175], v[194:195]
	v_pk_fma_f32 v[46:47], v[46:47], v[172:173], v[192:193]
	global_store_dwordx4 v[212:213], v[46:49], off offset:576
	v_pk_fma_f32 v[52:53], v[52:53], v[146:147], v[198:199]
	v_pk_fma_f32 v[50:51], v[50:51], v[144:145], v[196:197]
	global_store_dwordx4 v[214:215], v[50:53], off
	v_pk_fma_f32 v[44:45], v[44:45], v[156:157], v[202:203]
	v_pk_fma_f32 v[42:43], v[42:43], v[154:155], v[200:201]
	global_store_dwordx4 v[214:215], v[42:45], off offset:64
	v_pk_fma_f32 v[40:41], v[40:41], v[162:163], v[206:207]
	v_pk_fma_f32 v[38:39], v[38:39], v[160:161], v[204:205]
	global_store_dwordx4 v[214:215], v[38:41], off offset:512
	v_pk_fma_f32 v[32:33], v[32:33], v[174:175], v[210:211]
	v_pk_fma_f32 v[30:31], v[30:31], v[172:173], v[208:209]
	global_store_dwordx4 v[214:215], v[30:33], off offset:576
	v_add_co_u32_e32 v164, vcc, 0x140000, v166
	s_nop 1
	v_addc_co_u32_e32 v165, vcc, 0, v167, vcc
	global_load_dwordx4 v[176:179], v[164:165], off
	global_load_dwordx4 v[180:183], v[164:165], off offset:64
	global_load_dwordx4 v[184:187], v[164:165], off offset:512
	global_load_dwordx4 v[192:195], v[164:165], off offset:576
	v_add_co_u32_e32 v188, vcc, 0x160000, v166
	s_nop 1
	v_addc_co_u32_e32 v189, vcc, 0, v167, vcc
	global_load_dwordx4 v[196:199], v[188:189], off
	global_load_dwordx4 v[200:203], v[188:189], off offset:64
	global_load_dwordx4 v[204:207], v[188:189], off offset:512
	global_load_dwordx4 v[208:211], v[188:189], off offset:576
	v_add_co_u32_e32 v212, vcc, 0x140000, v170
	s_nop 1
	v_addc_co_u32_e32 v213, vcc, 0, v171, vcc
	v_add_co_u32_e32 v214, vcc, 0x160000, v170
	s_nop 1
	v_addc_co_u32_e32 v215, vcc, 0, v171, vcc
	s_waitcnt vmcnt(0)
	v_pk_fma_f32 v[36:37], v[36:37], v[146:147], v[178:179]
	v_pk_fma_f32 v[34:35], v[34:35], v[144:145], v[176:177]
	global_store_dwordx4 v[212:213], v[34:37], off
	v_pk_fma_f32 v[28:29], v[28:29], v[156:157], v[182:183]
	v_pk_fma_f32 v[26:27], v[26:27], v[154:155], v[180:181]
	global_store_dwordx4 v[212:213], v[26:29], off offset:64
	v_pk_fma_f32 v[24:25], v[24:25], v[162:163], v[186:187]
	v_pk_fma_f32 v[22:23], v[22:23], v[160:161], v[184:185]
	global_store_dwordx4 v[212:213], v[22:25], off offset:512
	v_pk_fma_f32 v[16:17], v[16:17], v[174:175], v[194:195]
	v_pk_fma_f32 v[14:15], v[14:15], v[172:173], v[192:193]
	global_store_dwordx4 v[212:213], v[14:17], off offset:576
	v_pk_fma_f32 v[20:21], v[20:21], v[146:147], v[198:199]
	v_pk_fma_f32 v[18:19], v[18:19], v[144:145], v[196:197]
	global_store_dwordx4 v[214:215], v[18:21], off
	v_pk_fma_f32 v[12:13], v[12:13], v[156:157], v[202:203]
	v_pk_fma_f32 v[10:11], v[10:11], v[154:155], v[200:201]
	global_store_dwordx4 v[214:215], v[10:13], off offset:64
	v_pk_fma_f32 v[8:9], v[8:9], v[162:163], v[206:207]
	v_pk_fma_f32 v[6:7], v[6:7], v[160:161], v[204:205]
	global_store_dwordx4 v[214:215], v[6:9], off offset:512
	v_pk_fma_f32 v[4:5], v[4:5], v[174:175], v[210:211]
	v_pk_fma_f32 v[2:3], v[2:3], v[172:173], v[208:209]
	global_store_dwordx4 v[214:215], v[2:5], off offset:576
	s_mov_b32 s48, s12
	s_mov_b32 s20, s14
	s_mov_b64 s[24:25], s[18:19]
	s_mov_b64 s[22:23], s[16:17]
	v_readlane_b32 s50, v250, 9
	v_readlane_b32 s51, v250, 10
	v_readlane_b32 s54, v250, 13
	v_readlane_b32 s55, v250, 14
	v_readlane_b32 s56, v250, 15
	v_readlane_b32 s57, v250, 16
	v_readlane_b32 s58, v250, 17
	v_readlane_b32 s59, v250, 18
	v_readlane_b32 s60, v250, 19
	v_readlane_b32 s61, v250, 20
	v_readlane_b32 s62, v250, 21
	v_readlane_b32 s63, v250, 22
	s_and_b64 vcc, exec, s[0:1]
	s_cbranch_vccz .LBB0_1284
	s_waitcnt vmcnt(0)
	s_cmpk_gt_u32 s30, 0xff
	s_cbranch_scc1 .LBB0_1291
	s_barrier

.LBB0_3319:
	ds_read_b128 v[144:147], v152
	ds_read_b128 v[158:161], v152 offset:1024
	ds_read_b128 v[162:165], v152 offset:2048
	ds_read_b128 v[166:169], v152 offset:3072
	s_add_u32 s36, s34, 0xfff80080
	s_addc_u32 s37, s35, -1
	s_cmp_eq_u32 s69, 28
	s_cselect_b32 s39, s25, s37
	s_cselect_b32 s38, s65, s36
	s_cselect_b32 s37, s23, s68
	s_cselect_b32 s36, s66, s67
	v_lshl_add_u64 v[148:149], s[34:35], 0, v[136:137]
	s_add_i32 m0, s31, 0xc000
	ds_read_b128 v[170:173], v153
	ds_read_b128 v[174:177], v153 offset:1024
	ds_read_b128 v[178:181], v153 offset:2048
	ds_read_b128 v[182:185], v153 offset:3072
	ds_read_b128 v[186:189], v153 offset:4096
	ds_read_b128 v[190:193], v153 offset:5120
	ds_read_b128 v[194:197], v153 offset:6144
	ds_read_b128 v[198:201], v153 offset:7168
	global_load_lds_dwordx4 v[148:149], off
	v_lshl_add_u64 v[148:149], s[34:35], 0, v[138:139]
	s_add_i32 m0, s31, 0xe000
	s_nop 0
	global_load_lds_dwordx4 v[148:149], off
	s_waitcnt lgkmcnt(8)
	s_barrier
	s_waitcnt lgkmcnt(0)
	s_setprio 1
	s_waitcnt lgkmcnt(0)
	v_mfma_f32_16x16x32_bf16 v[126:129], v[144:147], v[170:173], v[126:129]
	v_mfma_f32_16x16x32_bf16 v[122:125], v[162:165], v[170:173], v[122:125]
	v_mfma_f32_16x16x32_bf16 v[110:113], v[144:147], v[178:181], v[110:113]
	v_mfma_f32_16x16x32_bf16 v[106:109], v[162:165], v[178:181], v[106:109]
	v_mfma_f32_16x16x32_bf16 v[94:97], v[144:147], v[186:189], v[94:97]
	v_mfma_f32_16x16x32_bf16 v[90:93], v[162:165], v[186:189], v[90:93]
	v_mfma_f32_16x16x32_bf16 v[78:81], v[144:147], v[194:197], v[78:81]
	v_mfma_f32_16x16x32_bf16 v[74:77], v[162:165], v[194:197], v[74:77]
	v_mfma_f32_16x16x32_bf16 v[126:129], v[158:161], v[174:177], v[126:129]
	v_mfma_f32_16x16x32_bf16 v[122:125], v[166:169], v[174:177], v[122:125]
	v_mfma_f32_16x16x32_bf16 v[110:113], v[158:161], v[182:185], v[110:113]
	v_mfma_f32_16x16x32_bf16 v[106:109], v[166:169], v[182:185], v[106:109]
	v_mfma_f32_16x16x32_bf16 v[94:97], v[158:161], v[190:193], v[94:97]
	v_mfma_f32_16x16x32_bf16 v[90:93], v[166:169], v[190:193], v[90:93]
	v_mfma_f32_16x16x32_bf16 v[78:81], v[158:161], v[198:201], v[78:81]
	v_mfma_f32_16x16x32_bf16 v[74:77], v[166:169], v[198:201], v[74:77]
	s_setprio 0
	s_barrier
	s_add_i32 s70, s55, s46
	v_lshl_add_u64 v[148:149], s[36:37], 0, v[132:133]
	s_mov_b32 m0, s70
	ds_read_b128 v[202:205], v154
	ds_read_b128 v[206:209], v154 offset:1024
	ds_read_b128 v[210:213], v154 offset:2048
	ds_read_b128 v[214:217], v154 offset:3072
	global_load_lds_dwordx4 v[148:149], off
	v_lshl_add_u64 v[218:219], s[36:37], 0, v[130:131]
	s_add_i32 m0, s70, 0x2000
	s_nop 0
	global_load_lds_dwordx4 v[218:219], off
	s_barrier
	s_waitcnt lgkmcnt(0)
	s_setprio 1
	s_waitcnt lgkmcnt(0)
	v_mfma_f32_16x16x32_bf16 v[118:121], v[202:205], v[170:173], v[118:121]
	v_mfma_f32_16x16x32_bf16 v[114:117], v[210:213], v[170:173], v[114:117]
	v_mfma_f32_16x16x32_bf16 v[102:105], v[202:205], v[178:181], v[102:105]
	v_mfma_f32_16x16x32_bf16 v[98:101], v[210:213], v[178:181], v[98:101]
	v_mfma_f32_16x16x32_bf16 v[86:89], v[202:205], v[186:189], v[86:89]
	v_mfma_f32_16x16x32_bf16 v[82:85], v[210:213], v[186:189], v[82:85]
	v_mfma_f32_16x16x32_bf16 v[70:73], v[202:205], v[194:197], v[70:73]
	v_mfma_f32_16x16x32_bf16 v[66:69], v[210:213], v[194:197], v[66:69]
	v_mfma_f32_16x16x32_bf16 v[118:121], v[206:209], v[174:177], v[118:121]
	v_mfma_f32_16x16x32_bf16 v[114:117], v[214:217], v[174:177], v[114:117]
	v_mfma_f32_16x16x32_bf16 v[102:105], v[206:209], v[182:185], v[102:105]
	v_mfma_f32_16x16x32_bf16 v[98:101], v[214:217], v[182:185], v[98:101]
	v_mfma_f32_16x16x32_bf16 v[86:89], v[206:209], v[190:193], v[86:89]
	v_mfma_f32_16x16x32_bf16 v[82:85], v[214:217], v[190:193], v[82:85]
	v_mfma_f32_16x16x32_bf16 v[70:73], v[206:209], v[198:201], v[70:73]
	v_mfma_f32_16x16x32_bf16 v[66:69], v[214:217], v[198:201], v[66:69]
	s_setprio 0
	s_mov_b32 m0, s31
	v_lshl_add_u64 v[220:221], s[38:39], 0, v[132:133]
	s_barrier
	ds_read_b128 v[170:173], v153 offset:16384
	ds_read_b128 v[174:177], v153 offset:17408
	ds_read_b128 v[178:181], v153 offset:18432
	ds_read_b128 v[182:185], v153 offset:19456
	ds_read_b128 v[186:189], v153 offset:20480
	ds_read_b128 v[190:193], v153 offset:21504
	ds_read_b128 v[194:197], v153 offset:22528
	ds_read_b128 v[198:201], v153 offset:23552
	global_load_lds_dwordx4 v[220:221], off
	v_lshl_add_u64 v[222:223], s[38:39], 0, v[130:131]
	s_mov_b32 m0, s48
	s_nop 0
	global_load_lds_dwordx4 v[222:223], off
	s_barrier
	s_waitcnt lgkmcnt(0)
	s_setprio 1
	s_waitcnt lgkmcnt(0)
	v_mfma_f32_16x16x32_bf16 v[62:65], v[144:147], v[170:173], v[62:65]
	v_mfma_f32_16x16x32_bf16 v[58:61], v[162:165], v[170:173], v[58:61]
	v_mfma_f32_16x16x32_bf16 v[46:49], v[144:147], v[178:181], v[46:49]
	v_mfma_f32_16x16x32_bf16 v[42:45], v[162:165], v[178:181], v[42:45]
	v_mfma_f32_16x16x32_bf16 v[30:33], v[144:147], v[186:189], v[30:33]
	v_mfma_f32_16x16x32_bf16 v[26:29], v[162:165], v[186:189], v[26:29]
	v_mfma_f32_16x16x32_bf16 v[22:25], v[144:147], v[194:197], v[22:25]
	v_mfma_f32_16x16x32_bf16 v[14:17], v[162:165], v[194:197], v[14:17]
	v_mfma_f32_16x16x32_bf16 v[62:65], v[158:161], v[174:177], v[62:65]
	v_mfma_f32_16x16x32_bf16 v[58:61], v[166:169], v[174:177], v[58:61]
	v_mfma_f32_16x16x32_bf16 v[46:49], v[158:161], v[182:185], v[46:49]
	v_mfma_f32_16x16x32_bf16 v[42:45], v[166:169], v[182:185], v[42:45]
	v_mfma_f32_16x16x32_bf16 v[30:33], v[158:161], v[190:193], v[30:33]
	v_mfma_f32_16x16x32_bf16 v[26:29], v[166:169], v[190:193], v[26:29]
	v_mfma_f32_16x16x32_bf16 v[22:25], v[158:161], v[198:201], v[22:25]
	v_mfma_f32_16x16x32_bf16 v[14:17], v[166:169], v[198:201], v[14:17]
	s_setprio 0
	s_barrier
	s_add_u32 s70, s36, 0x80000
	s_addc_u32 s71, s37, 0
	s_add_i32 s72, s56, s46
	v_lshl_add_u64 v[144:145], s[70:71], 0, v[132:133]
	s_mov_b32 m0, s72
	s_nop 0
	global_load_lds_dwordx4 v[144:145], off
	v_lshl_add_u64 v[144:145], s[70:71], 0, v[130:131]
	s_add_i32 m0, s72, 0x2000
	s_nop 0
	global_load_lds_dwordx4 v[144:145], off
	s_waitcnt vmcnt(6)
	s_barrier
	s_setprio 1
	v_mfma_f32_16x16x32_bf16 v[54:57], v[202:205], v[170:173], v[54:57]
	v_mfma_f32_16x16x32_bf16 v[50:53], v[210:213], v[170:173], v[50:53]
	v_mfma_f32_16x16x32_bf16 v[38:41], v[202:205], v[178:181], v[38:41]
	v_mfma_f32_16x16x32_bf16 v[34:37], v[210:213], v[178:181], v[34:37]
	v_mfma_f32_16x16x32_bf16 v[18:21], v[202:205], v[186:189], v[18:21]
	v_mfma_f32_16x16x32_bf16 v[10:13], v[210:213], v[186:189], v[10:13]
	v_mfma_f32_16x16x32_bf16 v[6:9], v[202:205], v[194:197], v[6:9]
	v_mfma_f32_16x16x32_bf16 v[2:5], v[210:213], v[194:197], v[2:5]
	v_mfma_f32_16x16x32_bf16 v[54:57], v[206:209], v[174:177], v[54:57]
	v_mfma_f32_16x16x32_bf16 v[50:53], v[214:217], v[174:177], v[50:53]
	v_mfma_f32_16x16x32_bf16 v[38:41], v[206:209], v[182:185], v[38:41]
	v_mfma_f32_16x16x32_bf16 v[34:37], v[214:217], v[182:185], v[34:37]
	v_mfma_f32_16x16x32_bf16 v[18:21], v[206:209], v[190:193], v[18:21]
	v_mfma_f32_16x16x32_bf16 v[10:13], v[214:217], v[190:193], v[10:13]
	v_mfma_f32_16x16x32_bf16 v[6:9], v[206:209], v[198:201], v[6:9]
	v_mfma_f32_16x16x32_bf16 v[2:5], v[214:217], v[198:201], v[2:5]
	s_setprio 0
	s_add_i32 s70, 0, 0x18000
	v_add_u32_e32 v134, s70, v150
	s_barrier
	ds_read_b128 v[144:147], v134
	ds_read_b128 v[158:161], v134 offset:1024
	ds_read_b128 v[162:165], v134 offset:2048
	ds_read_b128 v[166:169], v134 offset:3072
	s_add_u32 s38, s38, 0x80000
	s_addc_u32 s39, s39, 0
	s_mov_b32 m0, s49
	v_lshl_add_u64 v[202:203], s[38:39], 0, v[132:133]
	ds_read_b128 v[170:173], v153 offset:32768
	ds_read_b128 v[174:177], v153 offset:33792
	ds_read_b128 v[178:181], v153 offset:34816
	ds_read_b128 v[182:185], v153 offset:35840
	ds_read_b128 v[186:189], v153 offset:36864
	ds_read_b128 v[190:193], v153 offset:37888
	ds_read_b128 v[194:197], v153 offset:38912
	ds_read_b128 v[198:201], v153 offset:39936
	global_load_lds_dwordx4 v[202:203], off
	v_lshl_add_u64 v[202:203], s[38:39], 0, v[130:131]
	s_mov_b32 m0, s50
	s_nop 0
	global_load_lds_dwordx4 v[202:203], off
	s_waitcnt lgkmcnt(8)
	s_barrier
	s_waitcnt lgkmcnt(0)
	s_setprio 1
	s_waitcnt lgkmcnt(0)
	v_mfma_f32_16x16x32_bf16 v[126:129], v[144:147], v[170:173], v[126:129]
	v_mfma_f32_16x16x32_bf16 v[122:125], v[162:165], v[170:173], v[122:125]
	v_mfma_f32_16x16x32_bf16 v[110:113], v[144:147], v[178:181], v[110:113]
	v_mfma_f32_16x16x32_bf16 v[106:109], v[162:165], v[178:181], v[106:109]
	v_mfma_f32_16x16x32_bf16 v[94:97], v[144:147], v[186:189], v[94:97]
	v_mfma_f32_16x16x32_bf16 v[90:93], v[162:165], v[186:189], v[90:93]
	v_mfma_f32_16x16x32_bf16 v[78:81], v[144:147], v[194:197], v[78:81]
	v_mfma_f32_16x16x32_bf16 v[74:77], v[162:165], v[194:197], v[74:77]
	v_mfma_f32_16x16x32_bf16 v[126:129], v[158:161], v[174:177], v[126:129]
	v_mfma_f32_16x16x32_bf16 v[122:125], v[166:169], v[174:177], v[122:125]
	v_mfma_f32_16x16x32_bf16 v[110:113], v[158:161], v[182:185], v[110:113]
	v_mfma_f32_16x16x32_bf16 v[106:109], v[166:169], v[182:185], v[106:109]
	v_mfma_f32_16x16x32_bf16 v[94:97], v[158:161], v[190:193], v[94:97]
	v_mfma_f32_16x16x32_bf16 v[90:93], v[166:169], v[190:193], v[90:93]
	v_mfma_f32_16x16x32_bf16 v[78:81], v[158:161], v[198:201], v[78:81]
	v_mfma_f32_16x16x32_bf16 v[74:77], v[166:169], v[198:201], v[74:77]
	s_setprio 0
	s_barrier
	s_add_i32 s38, 0, 0x1c000
	s_add_i32 s39, s70, s46
	v_add_u32_e32 v134, s38, v150
	v_lshl_add_u64 v[148:149], v[148:149], 0, s[6:7]
	s_mov_b32 m0, s39
	ds_read_b128 v[202:205], v134
	ds_read_b128 v[206:209], v134 offset:1024
	ds_read_b128 v[210:213], v134 offset:2048
	ds_read_b128 v[214:217], v134 offset:3072
	global_load_lds_dwordx4 v[148:149], off
	v_lshl_add_u64 v[148:149], v[218:219], 0, s[6:7]
	s_add_i32 m0, s39, 0x2000
	s_nop 0
	global_load_lds_dwordx4 v[148:149], off
	s_barrier
	s_waitcnt lgkmcnt(0)
	s_setprio 1
	s_waitcnt lgkmcnt(0)
	v_mfma_f32_16x16x32_bf16 v[118:121], v[202:205], v[170:173], v[118:121]
	v_mfma_f32_16x16x32_bf16 v[114:117], v[210:213], v[170:173], v[114:117]
	v_mfma_f32_16x16x32_bf16 v[102:105], v[202:205], v[178:181], v[102:105]
	v_mfma_f32_16x16x32_bf16 v[98:101], v[210:213], v[178:181], v[98:101]
	v_mfma_f32_16x16x32_bf16 v[86:89], v[202:205], v[186:189], v[86:89]
	v_mfma_f32_16x16x32_bf16 v[82:85], v[210:213], v[186:189], v[82:85]
	v_mfma_f32_16x16x32_bf16 v[70:73], v[202:205], v[194:197], v[70:73]
	v_mfma_f32_16x16x32_bf16 v[66:69], v[210:213], v[194:197], v[66:69]
	v_mfma_f32_16x16x32_bf16 v[118:121], v[206:209], v[174:177], v[118:121]
	v_mfma_f32_16x16x32_bf16 v[114:117], v[214:217], v[174:177], v[114:117]
	v_mfma_f32_16x16x32_bf16 v[102:105], v[206:209], v[182:185], v[102:105]
	v_mfma_f32_16x16x32_bf16 v[98:101], v[214:217], v[182:185], v[98:101]
	v_mfma_f32_16x16x32_bf16 v[86:89], v[206:209], v[190:193], v[86:89]
	v_mfma_f32_16x16x32_bf16 v[82:85], v[214:217], v[190:193], v[82:85]
	v_mfma_f32_16x16x32_bf16 v[70:73], v[206:209], v[198:201], v[70:73]
	v_mfma_f32_16x16x32_bf16 v[66:69], v[214:217], v[198:201], v[66:69]
	s_setprio 0
	s_mov_b32 m0, s52
	v_lshl_add_u64 v[148:149], v[220:221], 0, s[6:7]
	s_barrier
	ds_read_b128 v[170:173], v153 offset:49152
	ds_read_b128 v[174:177], v153 offset:50176
	ds_read_b128 v[178:181], v153 offset:51200
	ds_read_b128 v[182:185], v153 offset:52224
	ds_read_b128 v[186:189], v153 offset:53248
	ds_read_b128 v[190:193], v153 offset:54272
	ds_read_b128 v[194:197], v153 offset:55296
	ds_read_b128 v[198:201], v153 offset:56320
	global_load_lds_dwordx4 v[148:149], off
	v_lshl_add_u64 v[148:149], v[222:223], 0, s[6:7]
	s_mov_b32 m0, s53
	s_nop 0
	global_load_lds_dwordx4 v[148:149], off
	s_barrier
	s_waitcnt lgkmcnt(0)
	s_setprio 1
	s_waitcnt lgkmcnt(0)
	v_mfma_f32_16x16x32_bf16 v[62:65], v[144:147], v[170:173], v[62:65]
	v_mfma_f32_16x16x32_bf16 v[58:61], v[162:165], v[170:173], v[58:61]
	v_mfma_f32_16x16x32_bf16 v[46:49], v[144:147], v[178:181], v[46:49]
	v_mfma_f32_16x16x32_bf16 v[42:45], v[162:165], v[178:181], v[42:45]
	v_mfma_f32_16x16x32_bf16 v[30:33], v[144:147], v[186:189], v[30:33]
	v_mfma_f32_16x16x32_bf16 v[26:29], v[162:165], v[186:189], v[26:29]
	v_mfma_f32_16x16x32_bf16 v[22:25], v[144:147], v[194:197], v[22:25]
	v_mfma_f32_16x16x32_bf16 v[14:17], v[162:165], v[194:197], v[14:17]
	v_mfma_f32_16x16x32_bf16 v[62:65], v[158:161], v[174:177], v[62:65]
	v_mfma_f32_16x16x32_bf16 v[58:61], v[166:169], v[174:177], v[58:61]
	v_mfma_f32_16x16x32_bf16 v[46:49], v[158:161], v[182:185], v[46:49]
	v_mfma_f32_16x16x32_bf16 v[42:45], v[166:169], v[182:185], v[42:45]
	v_mfma_f32_16x16x32_bf16 v[30:33], v[158:161], v[190:193], v[30:33]
	v_mfma_f32_16x16x32_bf16 v[26:29], v[166:169], v[190:193], v[26:29]
	v_mfma_f32_16x16x32_bf16 v[22:25], v[158:161], v[198:201], v[22:25]
	v_mfma_f32_16x16x32_bf16 v[14:17], v[166:169], v[198:201], v[14:17]
	s_setprio 0
	s_barrier
	s_add_u32 s36, s36, 0x80080
	s_addc_u32 s37, s37, 0
	s_add_i32 s38, s38, s46
	v_lshl_add_u64 v[144:145], s[36:37], 0, v[132:133]
	s_mov_b32 m0, s38
	s_nop 0
	global_load_lds_dwordx4 v[144:145], off
	v_lshl_add_u64 v[144:145], s[36:37], 0, v[130:131]
	s_add_i32 m0, s38, 0x2000
	s_nop 0
	global_load_lds_dwordx4 v[144:145], off
	s_waitcnt vmcnt(6)
	s_barrier
	s_setprio 1
	v_mfma_f32_16x16x32_bf16 v[54:57], v[202:205], v[170:173], v[54:57]
	v_mfma_f32_16x16x32_bf16 v[50:53], v[210:213], v[170:173], v[50:53]
	v_mfma_f32_16x16x32_bf16 v[38:41], v[202:205], v[178:181], v[38:41]
	v_mfma_f32_16x16x32_bf16 v[34:37], v[210:213], v[178:181], v[34:37]
	v_mfma_f32_16x16x32_bf16 v[18:21], v[202:205], v[186:189], v[18:21]
	v_mfma_f32_16x16x32_bf16 v[10:13], v[210:213], v[186:189], v[10:13]
	v_mfma_f32_16x16x32_bf16 v[6:9], v[202:205], v[194:197], v[6:9]
	v_mfma_f32_16x16x32_bf16 v[2:5], v[210:213], v[194:197], v[2:5]
	v_mfma_f32_16x16x32_bf16 v[54:57], v[206:209], v[174:177], v[54:57]
	v_mfma_f32_16x16x32_bf16 v[50:53], v[214:217], v[174:177], v[50:53]
	v_mfma_f32_16x16x32_bf16 v[38:41], v[206:209], v[182:185], v[38:41]
	v_mfma_f32_16x16x32_bf16 v[34:37], v[214:217], v[182:185], v[34:37]
	v_mfma_f32_16x16x32_bf16 v[18:21], v[206:209], v[190:193], v[18:21]
	v_mfma_f32_16x16x32_bf16 v[10:13], v[214:217], v[190:193], v[10:13]
	v_mfma_f32_16x16x32_bf16 v[6:9], v[206:209], v[198:201], v[6:9]
	v_mfma_f32_16x16x32_bf16 v[2:5], v[214:217], v[198:201], v[2:5]
	s_setprio 0
	s_add_i32 s69, s69, 2
	s_add_u32 s34, s34, 0x100
	s_addc_u32 s35, s35, 0
	s_add_u32 s67, s67, 0x100
	s_addc_u32 s68, s68, 0
	s_cmp_gt_u32 s69, 29
	s_barrier
	s_cbranch_scc0 .LBB0_3319
	v_lshl_add_u32 v146, s30, 8, v1
	v_lshl_or_b32 v144, s64, 8, v151
	v_ashrrev_i32_e32 v147, 31, v146
	s_movk_i32 s23, 0x3fff
	v_ashrrev_i32_e32 v145, 31, v144
	v_lshlrev_b64 v[148:149], 13, v[146:147]
	v_cmp_lt_i32_e32 vcc, s23, v146
	v_lshl_add_u64 v[158:159], s[8:9], 0, v[148:149]
	v_lshlrev_b64 v[144:145], 2, v[144:145]
	v_cndmask_b32_e32 v134, v155, v156, vcc
	v_lshl_add_u64 v[174:175], v[158:159], 0, v[144:145]
	v_lshl_add_u64 v[158:159], s[4:5], 0, v[134:135]
	v_lshl_add_u64 v[166:167], v[158:159], 0, v[144:145]
	v_add_co_u32_e32 v162, vcc, s57, v166
	s_nop 1
	v_addc_co_u32_e32 v163, vcc, 0, v167, vcc
	v_lshl_add_u64 v[170:171], s[10:11], 0, v[148:149]
	v_lshl_add_u64 v[180:181], v[170:171], 0, v[144:145]
	v_lshl_add_u64 v[178:179], v[166:167], 0, s[12:13]
	global_load_dwordx4 v[144:147], v[162:163], off
	global_load_dwordx4 v[158:161], v[178:179], off offset:64
	global_load_dwordx4 v[164:167], v[178:179], off offset:512
	global_load_dwordx4 v[168:171], v[178:179], off offset:576
	global_load_dwordx4 v[182:185], v[174:175], off
	global_load_dwordx4 v[186:189], v[174:175], off offset:64
	global_load_dwordx4 v[190:193], v[174:175], off offset:512
	global_load_dwordx4 v[194:197], v[174:175], off offset:576
	v_add_co_u32_e32 v172, vcc, 0x20000, v174
	s_nop 1
	v_addc_co_u32_e32 v173, vcc, 0, v175, vcc
	global_load_dwordx4 v[198:201], v[172:173], off
	global_load_dwordx4 v[202:205], v[172:173], off offset:64
	global_load_dwordx4 v[206:209], v[172:173], off offset:512
	global_load_dwordx4 v[210:213], v[172:173], off offset:576
	v_add_co_u32_e32 v214, vcc, 0x20000, v180
	s_nop 1
	v_addc_co_u32_e32 v215, vcc, 0, v181, vcc
	s_waitcnt vmcnt(0)
	v_pk_fma_f32 v[128:129], v[128:129], v[146:147], v[184:185]
	v_pk_fma_f32 v[126:127], v[126:127], v[144:145], v[182:183]
	global_store_dwordx4 v[180:181], v[126:129], off
	v_pk_fma_f32 v[124:125], v[124:125], v[160:161], v[188:189]
	v_pk_fma_f32 v[122:123], v[122:123], v[158:159], v[186:187]
	global_store_dwordx4 v[180:181], v[122:125], off offset:64
	v_pk_fma_f32 v[120:121], v[120:121], v[166:167], v[192:193]
	v_pk_fma_f32 v[118:119], v[118:119], v[164:165], v[190:191]
	global_store_dwordx4 v[180:181], v[118:121], off offset:512
	v_pk_fma_f32 v[116:117], v[116:117], v[170:171], v[196:197]
	v_pk_fma_f32 v[114:115], v[114:115], v[168:169], v[194:195]
	global_store_dwordx4 v[180:181], v[114:117], off offset:576
	v_pk_fma_f32 v[112:113], v[112:113], v[146:147], v[200:201]
	v_pk_fma_f32 v[110:111], v[110:111], v[144:145], v[198:199]
	global_store_dwordx4 v[214:215], v[110:113], off
	v_pk_fma_f32 v[108:109], v[108:109], v[160:161], v[204:205]
	v_pk_fma_f32 v[106:107], v[106:107], v[158:159], v[202:203]
	global_store_dwordx4 v[214:215], v[106:109], off offset:64
	v_pk_fma_f32 v[104:105], v[104:105], v[166:167], v[208:209]
	v_pk_fma_f32 v[102:103], v[102:103], v[164:165], v[206:207]
	global_store_dwordx4 v[214:215], v[102:105], off offset:512
	v_pk_fma_f32 v[100:101], v[100:101], v[170:171], v[212:213]
	v_pk_fma_f32 v[98:99], v[98:99], v[168:169], v[210:211]
	global_store_dwordx4 v[214:215], v[98:101], off offset:576
	v_add_co_u32_e32 v148, vcc, 0x40000, v174
	s_nop 1
	v_addc_co_u32_e32 v149, vcc, 0, v175, vcc
	global_load_dwordx4 v[182:185], v[148:149], off
	global_load_dwordx4 v[186:189], v[148:149], off offset:64
	global_load_dwordx4 v[190:193], v[148:149], off offset:512
	global_load_dwordx4 v[194:197], v[148:149], off offset:576
	v_add_co_u32_e32 v172, vcc, 0x60000, v174
	s_nop 1
	v_addc_co_u32_e32 v173, vcc, 0, v175, vcc
	global_load_dwordx4 v[198:201], v[172:173], off
	global_load_dwordx4 v[202:205], v[172:173], off offset:64
	global_load_dwordx4 v[206:209], v[172:173], off offset:512
	global_load_dwordx4 v[210:213], v[172:173], off offset:576
	v_add_co_u32_e32 v176, vcc, 0x40000, v180
	s_nop 1
	v_addc_co_u32_e32 v177, vcc, 0, v181, vcc
	v_add_co_u32_e32 v214, vcc, 0x60000, v180
	s_nop 1
	v_addc_co_u32_e32 v215, vcc, 0, v181, vcc
	s_waitcnt vmcnt(0)
	v_pk_fma_f32 v[96:97], v[96:97], v[146:147], v[184:185]
	v_pk_fma_f32 v[94:95], v[94:95], v[144:145], v[182:183]
	global_store_dwordx4 v[176:177], v[94:97], off
	v_pk_fma_f32 v[92:93], v[92:93], v[160:161], v[188:189]
	v_pk_fma_f32 v[90:91], v[90:91], v[158:159], v[186:187]
	global_store_dwordx4 v[176:177], v[90:93], off offset:64
	v_pk_fma_f32 v[88:89], v[88:89], v[166:167], v[192:193]
	v_pk_fma_f32 v[86:87], v[86:87], v[164:165], v[190:191]
	global_store_dwordx4 v[176:177], v[86:89], off offset:512
	v_pk_fma_f32 v[84:85], v[84:85], v[170:171], v[196:197]
	v_pk_fma_f32 v[82:83], v[82:83], v[168:169], v[194:195]
	global_store_dwordx4 v[176:177], v[82:85], off offset:576
	v_pk_fma_f32 v[80:81], v[80:81], v[146:147], v[200:201]
	v_pk_fma_f32 v[78:79], v[78:79], v[144:145], v[198:199]
	global_store_dwordx4 v[214:215], v[78:81], off
	v_pk_fma_f32 v[76:77], v[76:77], v[160:161], v[204:205]
	v_pk_fma_f32 v[74:75], v[74:75], v[158:159], v[202:203]
	global_store_dwordx4 v[214:215], v[74:77], off offset:64
	v_pk_fma_f32 v[72:73], v[72:73], v[166:167], v[208:209]
	v_pk_fma_f32 v[70:71], v[70:71], v[164:165], v[206:207]
	global_store_dwordx4 v[214:215], v[70:73], off offset:512
	v_pk_fma_f32 v[68:69], v[68:69], v[170:171], v[212:213]
	v_pk_fma_f32 v[66:67], v[66:67], v[168:169], v[210:211]
	global_store_dwordx4 v[214:215], v[66:69], off offset:576
	v_add_co_u32_e32 v148, vcc, 0x100000, v174
	s_nop 1
	v_addc_co_u32_e32 v149, vcc, 0, v175, vcc
	global_load_dwordx4 v[182:185], v[148:149], off
	global_load_dwordx4 v[186:189], v[148:149], off offset:64
	global_load_dwordx4 v[190:193], v[148:149], off offset:512
	global_load_dwordx4 v[194:197], v[148:149], off offset:576
	v_add_co_u32_e32 v172, vcc, 0x120000, v174
	s_nop 1
	v_addc_co_u32_e32 v173, vcc, 0, v175, vcc
	global_load_dwordx4 v[198:201], v[172:173], off
	global_load_dwordx4 v[202:205], v[172:173], off offset:64
	global_load_dwordx4 v[206:209], v[172:173], off offset:512
	global_load_dwordx4 v[210:213], v[172:173], off offset:576
	v_add_co_u32_e32 v176, vcc, 0x100000, v180
	s_nop 1
	v_addc_co_u32_e32 v177, vcc, 0, v181, vcc
	v_add_co_u32_e32 v214, vcc, 0x120000, v180
	s_nop 1
	v_addc_co_u32_e32 v215, vcc, 0, v181, vcc
	s_waitcnt vmcnt(0)
	v_pk_fma_f32 v[64:65], v[64:65], v[146:147], v[184:185]
	v_pk_fma_f32 v[62:63], v[62:63], v[144:145], v[182:183]
	global_store_dwordx4 v[176:177], v[62:65], off
	v_pk_fma_f32 v[60:61], v[60:61], v[160:161], v[188:189]
	v_pk_fma_f32 v[58:59], v[58:59], v[158:159], v[186:187]
	global_store_dwordx4 v[176:177], v[58:61], off offset:64
	v_pk_fma_f32 v[56:57], v[56:57], v[166:167], v[192:193]
	v_pk_fma_f32 v[54:55], v[54:55], v[164:165], v[190:191]
	global_store_dwordx4 v[176:177], v[54:57], off offset:512
	v_pk_fma_f32 v[52:53], v[52:53], v[170:171], v[196:197]
	v_pk_fma_f32 v[50:51], v[50:51], v[168:169], v[194:195]
	global_store_dwordx4 v[176:177], v[50:53], off offset:576
	v_pk_fma_f32 v[48:49], v[48:49], v[146:147], v[200:201]
	v_pk_fma_f32 v[46:47], v[46:47], v[144:145], v[198:199]
	global_store_dwordx4 v[214:215], v[46:49], off
	v_pk_fma_f32 v[44:45], v[44:45], v[160:161], v[204:205]
	v_pk_fma_f32 v[42:43], v[42:43], v[158:159], v[202:203]
	global_store_dwordx4 v[214:215], v[42:45], off offset:64
	v_pk_fma_f32 v[40:41], v[40:41], v[166:167], v[208:209]
	v_pk_fma_f32 v[38:39], v[38:39], v[164:165], v[206:207]
	global_store_dwordx4 v[214:215], v[38:41], off offset:512
	v_pk_fma_f32 v[36:37], v[36:37], v[170:171], v[212:213]
	v_pk_fma_f32 v[34:35], v[34:35], v[168:169], v[210:211]
	global_store_dwordx4 v[214:215], v[34:37], off offset:576
	v_add_co_u32_e32 v148, vcc, 0x140000, v174
	s_nop 1
	v_addc_co_u32_e32 v149, vcc, 0, v175, vcc
	global_load_dwordx4 v[182:185], v[148:149], off
	global_load_dwordx4 v[186:189], v[148:149], off offset:64
	global_load_dwordx4 v[190:193], v[148:149], off offset:512
	global_load_dwordx4 v[194:197], v[148:149], off offset:576
	v_add_co_u32_e32 v172, vcc, 0x160000, v174
	s_nop 1
	v_addc_co_u32_e32 v173, vcc, 0, v175, vcc
	global_load_dwordx4 v[198:201], v[172:173], off
	global_load_dwordx4 v[202:205], v[172:173], off offset:64
	global_load_dwordx4 v[206:209], v[172:173], off offset:512
	global_load_dwordx4 v[210:213], v[172:173], off offset:576
	v_add_co_u32_e32 v176, vcc, 0x140000, v180
	s_nop 1
	v_addc_co_u32_e32 v177, vcc, 0, v181, vcc
	v_add_co_u32_e32 v214, vcc, 0x160000, v180
	s_nop 1
	v_addc_co_u32_e32 v215, vcc, 0, v181, vcc
	s_waitcnt vmcnt(0)
	v_pk_fma_f32 v[32:33], v[32:33], v[146:147], v[184:185]
	v_pk_fma_f32 v[30:31], v[30:31], v[144:145], v[182:183]
	global_store_dwordx4 v[176:177], v[30:33], off
	v_pk_fma_f32 v[28:29], v[28:29], v[160:161], v[188:189]
	v_pk_fma_f32 v[26:27], v[26:27], v[158:159], v[186:187]
	global_store_dwordx4 v[176:177], v[26:29], off offset:64
	v_pk_fma_f32 v[20:21], v[20:21], v[166:167], v[192:193]
	v_pk_fma_f32 v[18:19], v[18:19], v[164:165], v[190:191]
	global_store_dwordx4 v[176:177], v[18:21], off offset:512
	v_pk_fma_f32 v[12:13], v[12:13], v[170:171], v[196:197]
	v_pk_fma_f32 v[10:11], v[10:11], v[168:169], v[194:195]
	global_store_dwordx4 v[176:177], v[10:13], off offset:576
	v_pk_fma_f32 v[24:25], v[24:25], v[146:147], v[200:201]
	v_pk_fma_f32 v[22:23], v[22:23], v[144:145], v[198:199]
	global_store_dwordx4 v[214:215], v[22:25], off
	v_pk_fma_f32 v[16:17], v[16:17], v[160:161], v[204:205]
	v_pk_fma_f32 v[14:15], v[14:15], v[158:159], v[202:203]
	global_store_dwordx4 v[214:215], v[14:17], off offset:64
	v_pk_fma_f32 v[8:9], v[8:9], v[166:167], v[208:209]
	v_pk_fma_f32 v[6:7], v[6:7], v[164:165], v[206:207]
	global_store_dwordx4 v[214:215], v[6:9], off offset:512
	v_pk_fma_f32 v[4:5], v[4:5], v[170:171], v[212:213]
	v_pk_fma_f32 v[2:3], v[2:3], v[168:169], v[210:211]
	global_store_dwordx4 v[214:215], v[2:5], off offset:576
	s_mov_b32 s64, s22
	s_mov_b32 s30, s24
	s_mov_b64 s[36:37], s[28:29]
	s_mov_b64 s[34:35], s[26:27]
	s_and_b64 vcc, exec, s[0:1]
	s_cbranch_vccz .LBB0_3316
	s_waitcnt vmcnt(0)
	v_readlane_b32 s52, v250, 40
	s_cmpk_gt_u32 s41, 0xff
	v_readlane_b32 s53, v250, 41
	v_readlane_b32 s54, v250, 42
	v_readlane_b32 s55, v250, 43
	s_cbranch_scc1 .LBB0_3323
	s_barrier
